# scan staging waves: operand pairs built by two v_mov for one packed f32 op replaced by two scalar ops on the original registers (50 instructions fewer per chunk)
# baseline (speedup 1.0000x reference)
.LBB0_794:
	s_cmp_eq_u32 s51, 0
	s_cbranch_scc1 .LBB0_796
	s_add_i32 s44, s51, -1
	s_mul_hi_u32 s2, s44, 0xaaaaaaab
	s_lshr_b32 s2, s2, 1
	s_mul_i32 s2, s2, 3
	s_sub_i32 s2, s44, s2
	v_mov_b32_e32 v50, v124
	v_lshl_add_u32 v49, s2, 8, v170
	s_lshl_b32 s2, s2, 13
	s_lshl_b32 s53, s44, 13
	ds_read_b64 v[112:113], v49
	s_and_b32 s53, s53, 0x2000
	v_add_u32_e32 v49, s2, v177
	ds_read_b128 v[104:107], v49
	ds_read_b128 v[100:103], v49 offset:16
	v_add_u32_e32 v49, s53, v185
	ds_read_b128 v[108:111], v49
	ds_read_b128 v[116:119], v49 offset:16
	s_mov_b32 s53, 0x800000
	s_lshl_b32 s44, s44, 5
	s_waitcnt lgkmcnt(1)
	v_pk_fma_f32 v[130:131], v[112:113], v[104:105], v[108:109] op_sel_hi:[0,1,1]
	s_waitcnt lgkmcnt(0)
	v_pk_fma_f32 v[116:117], v[112:113], v[100:101], v[116:117] op_sel_hi:[0,1,1]
	v_pk_fma_f32 v[128:129], v[112:113], v[106:107], v[110:111] op_sel_hi:[0,1,1]
	v_pk_fma_f32 v[114:115], v[112:113], v[102:103], v[118:119] op_sel_hi:[0,1,1]
	v_add_f32_e32 v108, v130, v131
	v_add_f32_e32 v109, v116, v117
	v_add_f32_e32 v110, v128, v129
	v_add_f32_e32 v111, v114, v115
	s_nop 0
	v_pk_add_f32 v[108:109], v[108:109], v[110:111]
	s_nop 0
	v_add_f32_e32 v49, 0, v108
	v_add_f32_e32 v49, v49, v109
	s_nop 1
	v_add_f32_dpp v49, v49, v49 row_half_mirror row_mask:0xf bank_mask:0xf bound_ctrl:1
	s_nop 1
	v_add_f32_dpp v49, v49, v49 quad_perm:[3,2,1,0] row_mask:0xf bank_mask:0xf bound_ctrl:1
	s_nop 1
	v_add_f32_dpp v49, v49, v49 quad_perm:[1,0,3,2] row_mask:0xf bank_mask:0xf bound_ctrl:1
	v_fmamk_f32 v131, v49, 0xbc800000, v131
	v_fmamk_f32 v117, v49, 0xbc800000, v117
	v_fmamk_f32 v129, v49, 0xbc800000, v129
	v_fmac_f32_e32 v130, 0xbc800000, v49
	v_fmamk_f32 v115, v49, 0xbc800000, v115
	v_fmac_f32_e32 v116, 0xbc800000, v49
	v_fmac_f32_e32 v128, 0xbc800000, v49
	v_fmac_f32_e32 v114, 0xbc800000, v49
	v_mul_f32_e32 v110, v131, v131
	v_mul_f32_e32 v111, v117, v117
	v_fma_f32 v108, v130, v130, v110
	v_fma_f32 v109, v116, v116, v111
	v_mul_f32_e32 v118, v129, v129
	v_mul_f32_e32 v119, v115, v115
	s_nop 0
	v_fma_f32 v110, v128, v128, v118
	v_fma_f32 v111, v114, v114, v119
	s_nop 0
	v_pk_add_f32 v[108:109], v[108:109], v[110:111]
	s_nop 0
	v_add_f32_e32 v49, v108, v109
	s_nop 1
	v_add_f32_dpp v49, v49, v49 row_half_mirror row_mask:0xf bank_mask:0xf bound_ctrl:1
	s_nop 1
	v_add_f32_dpp v49, v49, v49 quad_perm:[3,2,1,0] row_mask:0xf bank_mask:0xf bound_ctrl:1
	s_nop 1
	v_add_f32_dpp v49, v49, v49 quad_perm:[1,0,3,2] row_mask:0xf bank_mask:0xf bound_ctrl:1
	v_fmamk_f32 v49, v49, 0x3c800000, v191
	v_cmp_gt_f32_e32 vcc, s53, v49
	v_mul_f32_e32 v51, 0x4b800000, v49
	s_nop 0
	v_cndmask_b32_e32 v49, v49, v51, vcc
	v_rsq_f32_e32 v49, v49
	s_nop 0
	v_mul_f32_e32 v51, 0x45800000, v49
	v_cndmask_b32_e32 v118, v49, v51, vcc
	v_add_u32_e32 v49, s2, v169
	ds_read_b128 v[120:123], v49
	ds_read_b128 v[108:111], v49 offset:16
	v_add_u32_e32 v49, s34, v167
	v_pk_mul_f32 v[136:137], v[130:131], v[118:119] op_sel_hi:[1,0]
	v_pk_mul_f32 v[138:139], v[128:129], v[118:119] op_sel_hi:[1,0]
	ds_read_b128 v[128:131], v49
	v_add_u32_e32 v49, s33, v167
	ds_read_b128 v[132:135], v49
	s_waitcnt lgkmcnt(0)
	v_pk_fma_f32 v[128:129], v[128:129], v[136:137], v[132:133]
	s_nop 0
	v_pk_fma_f32 v[104:105], v[112:113], v[104:105], v[128:129] op_sel:[1,0,0]
	v_pk_fma_f32 v[130:131], v[130:131], v[138:139], v[134:135]
	v_pk_mul_f32 v[104:105], v[120:121], v[104:105]
	v_mov_b32_e32 v120, v48
	v_mul_f32_e32 v49, 0x41000000, v104
	v_mul_f32_e32 v51, 0x41000000, v105
	v_cvt_pk_fp8_f32 v120, v49, v51
	v_pk_fma_f32 v[106:107], v[112:113], v[106:107], v[130:131] op_sel:[1,0,0]
	v_add_u32_e32 v49, s34, v168
	v_pk_mul_f32 v[106:107], v[122:123], v[106:107]
	v_pk_mul_f32 v[122:123], v[114:115], v[118:119] op_sel_hi:[1,0]
	v_mul_f32_e32 v104, 0x41000000, v106
	v_mul_f32_e32 v105, 0x41000000, v107
	v_cvt_pk_fp8_f32 v120, v104, v105 op_sel:[0,0,1]
	ds_read_b128 v[104:107], v49
	v_add_u32_e32 v49, s33, v168
	v_pk_mul_f32 v[118:119], v[116:117], v[118:119] op_sel_hi:[1,0]
	ds_read_b128 v[114:117], v49
	v_mov_b32_e32 v121, v48
	s_waitcnt lgkmcnt(0)
	v_pk_fma_f32 v[104:105], v[104:105], v[118:119], v[114:115]
	s_nop 0
	v_pk_fma_f32 v[100:101], v[112:113], v[100:101], v[104:105] op_sel:[1,0,0]
	v_pk_fma_f32 v[106:107], v[106:107], v[122:123], v[116:117]
	v_pk_mul_f32 v[100:101], v[108:109], v[100:101]
	v_pk_fma_f32 v[102:103], v[112:113], v[102:103], v[106:107] op_sel:[1,0,0]
	v_mul_f32_e32 v100, 0x41000000, v100
	v_mul_f32_e32 v101, 0x41000000, v101
	v_cvt_pk_fp8_f32 v121, v100, v101
	v_pk_mul_f32 v[102:103], v[110:111], v[102:103]
	v_lshl_add_u64 v[100:101], v[126:127], 0, s[44:45]
	v_mul_f32_e32 v49, 0x41000000, v102
	v_mul_f32_e32 v51, 0x41000000, v103
	v_cvt_pk_fp8_f32 v121, v49, v51 op_sel:[0,0,1]
	v_lshlrev_b64 v[100:101], 10, v[100:101]
	v_lshl_add_u64 v[100:101], s[72:73], 0, v[100:101]
	v_ashrrev_i32_e32 v51, 31, v50
	v_lshl_add_u64 v[50:51], v[100:101], 0, v[50:51]
	global_store_dwordx2 v[50:51], v[120:121], off
.LBB0_796:
	s_andn2_b64 vcc, exec, s[14:15]
	s_mov_b32 s2, 64
	s_cbranch_vccnz .LBB0_805
	v_mov_b32_e32 v100, v124
	v_add_u32_e32 v108, s46, v167
	v_add_u32_e32 v100, s3, v167
	ds_read_b128 v[100:103], v100
	ds_read_b128 v[108:111], v108
	s_waitcnt vmcnt(9)
	v_lshlrev_b32_e32 v104, 16, v72
	v_and_b32_e32 v105, 0xffff0000, v72
	v_lshlrev_b32_e32 v106, 16, v73
	v_and_b32_e32 v107, 0xffff0000, v73
	s_waitcnt vmcnt(6)
	v_lshlrev_b32_e32 v49, 16, v80
	v_and_b32_e32 v122, 0xffff0000, v80
	v_lshlrev_b32_e32 v120, 16, v81
	v_and_b32_e32 v121, 0xffff0000, v81
	v_add_u32_e32 v146, s47, v167
	v_sub_f32_e32 v121, v121, v107
	v_sub_f32_e32 v120, v120, v106
	v_sub_f32_e32 v123, v122, v105
	v_sub_f32_e32 v122, v49, v104
	s_waitcnt lgkmcnt(1)
	v_pk_fma_f32 v[138:139], v[122:123], v[100:101], v[104:105]
	v_pk_fma_f32 v[140:141], v[120:121], v[102:103], v[106:107]
	v_add_u32_e32 v49, s48, v167
	ds_read_b128 v[104:107], v146
	ds_read_b128 v[100:103], v49
	v_lshlrev_b32_e32 v116, 16, v68
	v_and_b32_e32 v117, 0xffff0000, v68
	s_waitcnt vmcnt(5)
	v_lshlrev_b32_e32 v142, 16, v88
	v_and_b32_e32 v143, 0xffff0000, v88
	v_lshlrev_b32_e32 v118, 16, v69
	v_and_b32_e32 v119, 0xffff0000, v69
	v_lshlrev_b32_e32 v144, 16, v89
	v_and_b32_e32 v145, 0xffff0000, v89
	v_sub_f32_e32 v123, v143, v117
	v_sub_f32_e32 v122, v142, v116
	v_sub_f32_e32 v121, v145, v119
	v_sub_f32_e32 v120, v144, v118
	s_waitcnt lgkmcnt(2)
	v_pk_fma_f32 v[144:145], v[122:123], v[108:109], v[116:117]
	v_add_u32_e32 v49, s3, v168
	v_pk_fma_f32 v[146:147], v[120:121], v[110:111], v[118:119]
	s_waitcnt lgkmcnt(0)
	v_pk_mul_f32 v[142:143], v[144:145], v[100:101]
	v_add_u32_e32 v100, s46, v168
	ds_read_b128 v[108:111], v49
	ds_read_b128 v[116:119], v100
	v_add_u32_e32 v49, s47, v168
	v_add_u32_e32 v120, s48, v168
	v_pk_mul_f32 v[148:149], v[146:147], v[102:103]
	ds_read_b128 v[100:103], v49
	ds_read_b128 v[120:123], v120
	v_lshlrev_b32_e32 v130, 16, v70
	v_and_b32_e32 v131, 0xffff0000, v70
	v_lshlrev_b32_e32 v152, 16, v90
	v_and_b32_e32 v153, 0xffff0000, v90
	v_lshlrev_b32_e32 v134, 16, v71
	v_and_b32_e32 v135, 0xffff0000, v71
	v_lshlrev_b32_e32 v150, 16, v91
	v_and_b32_e32 v151, 0xffff0000, v91
	v_sub_f32_e32 v153, v153, v131
	v_sub_f32_e32 v152, v152, v130
	v_sub_f32_e32 v151, v151, v135
	v_sub_f32_e32 v150, v150, v134
	s_waitcnt lgkmcnt(2)
	v_pk_fma_f32 v[152:153], v[152:153], v[116:117], v[130:131]
	v_pk_fma_f32 v[150:151], v[150:151], v[118:119], v[134:135]
	s_waitcnt lgkmcnt(0)
	v_pk_mul_f32 v[156:157], v[152:153], v[120:121]
	v_pk_mul_f32 v[154:155], v[150:151], v[122:123]
	v_mul_f32_e32 v118, v143, v143
	v_mul_f32_e32 v119, v157, v157
	v_fma_f32 v116, v142, v142, v118
	v_fma_f32 v117, v156, v156, v119
	v_mul_f32_e32 v120, v149, v149
	v_mul_f32_e32 v121, v155, v155
	s_mov_b32 s2, 0xf800000
	v_fma_f32 v118, v148, v148, v120
	v_fma_f32 v119, v154, v154, v121
	v_lshlrev_b32_e32 v128, 16, v74
	v_pk_add_f32 v[116:117], v[116:117], v[118:119]
	v_and_b32_e32 v129, 0xffff0000, v74
	v_add_f32_e32 v49, v116, v117
	v_lshlrev_b32_e32 v158, 16, v82
	v_and_b32_e32 v159, 0xffff0000, v82
	v_add_f32_dpp v49, v49, v49 row_half_mirror row_mask:0xf bank_mask:0xf bound_ctrl:1
	v_sub_f32_e32 v119, v159, v129
	v_lshlrev_b32_e32 v132, 16, v75
	v_add_f32_dpp v49, v49, v49 quad_perm:[3,2,1,0] row_mask:0xf bank_mask:0xf bound_ctrl:1
	v_and_b32_e32 v133, 0xffff0000, v75
	v_lshlrev_b32_e32 v160, 16, v83
	v_add_f32_dpp v49, v49, v49 quad_perm:[1,0,3,2] row_mask:0xf bank_mask:0xf bound_ctrl:1
	v_mul_f32_e32 v116, 0x4f800000, v49
	v_cmp_gt_f32_e32 vcc, s2, v49
	v_and_b32_e32 v161, 0xffff0000, v83
	v_sub_f32_e32 v117, v161, v133
	v_cndmask_b32_e32 v49, v49, v116, vcc
	v_sqrt_f32_e32 v118, v49
	v_sub_f32_e32 v116, v160, v132
	s_waitcnt vmcnt(3)
	v_lshlrev_b32_e32 v50, 16, v92
	v_and_b32_e32 v51, 0xffff0000, v92
	v_add_u32_e32 v120, -1, v118
	v_fma_f32 v121, -v120, v118, v49
	v_cmp_ge_f32_e64 s[14:15], 0, v121
	v_add_u32_e32 v121, 1, v118
	v_lshlrev_b32_e32 v136, 16, v93
	v_cndmask_b32_e64 v120, v118, v120, s[14:15]
	v_fma_f32 v118, -v121, v118, v49
	v_cmp_lt_f32_e64 s[14:15], 0, v118
	v_and_b32_e32 v137, 0xffff0000, v93
	v_lshlrev_b32_e32 v112, 16, v94
	v_cndmask_b32_e64 v118, v120, v121, s[14:15]
	v_mul_f32_e32 v120, 0x37800000, v118
	v_cndmask_b32_e32 v118, v118, v120, vcc
	v_cmp_class_f32_e32 vcc, v49, v192
	v_and_b32_e32 v113, 0xffff0000, v94
	v_lshlrev_b32_e32 v114, 16, v95
	v_cndmask_b32_e32 v49, v118, v49, vcc
	v_max_f32_e32 v49, 0x2b8cbccc, v49
	v_div_scale_f32 v120, s[14:15], v49, v49, 1.0
	v_rcp_f32_e32 v121, v120
	v_sub_f32_e32 v118, v158, v128
	v_pk_fma_f32 v[130:131], v[118:119], v[108:109], v[128:129]
	v_pk_fma_f32 v[128:129], v[116:117], v[110:111], v[132:133]
	v_fma_f32 v108, -v120, v121, 1.0
	v_fmac_f32_e32 v121, v108, v121
	v_div_scale_f32 v108, vcc, 1.0, v49, 1.0
	v_mul_f32_e32 v109, v108, v121
	v_fma_f32 v110, -v120, v109, v108
	v_fmac_f32_e32 v109, v110, v121
	v_fma_f32 v108, -v120, v109, v108
	v_div_fmas_f32 v108, v108, v121, v109
	v_div_fixup_f32 v158, v108, v49, 1.0
	v_add_u32_e32 v49, s49, v167
	ds_read_b128 v[108:111], v49
	v_pk_add_f32 v[116:117], v[50:51], -1.0 op_sel_hi:[1,0]
	v_pk_add_f32 v[118:119], v[136:137], -1.0 op_sel_hi:[1,0]
	v_add_u32_e32 v49, s50, v167
	ds_read_b128 v[132:135], v49
	s_waitcnt lgkmcnt(1)
	v_pk_fma_f32 v[110:111], v[118:119], v[110:111], 1.0 op_sel_hi:[1,1,0]
	v_pk_fma_f32 v[108:109], v[116:117], v[108:109], 1.0 op_sel_hi:[1,1,0]
	v_add_u32_e32 v49, s49, v168
	v_pk_mul_f32 v[118:119], v[146:147], v[110:111]
	v_pk_mul_f32 v[116:117], v[144:145], v[108:109]
	ds_read_b128 v[108:111], v49
	v_pk_mul_f32 v[142:143], v[142:143], v[158:159] op_sel_hi:[1,0]
	v_and_b32_e32 v115, 0xffff0000, v95
	v_pk_mul_f32 v[194:195], v[148:149], v[158:159] op_sel_hi:[1,0]
	v_pk_mul_f32 v[120:121], v[142:143], v[50:51]
	v_pk_mul_f32 v[50:51], v[156:157], v[158:159] op_sel_hi:[1,0]
	v_pk_add_f32 v[144:145], v[112:113], -1.0 op_sel_hi:[1,0]
	v_pk_mul_f32 v[122:123], v[194:195], v[136:137]
	v_pk_mul_f32 v[136:137], v[154:155], v[158:159] op_sel_hi:[1,0]
	v_pk_add_f32 v[154:155], v[114:115], -1.0 op_sel_hi:[1,0]
	s_waitcnt lgkmcnt(0)
	v_pk_fma_f32 v[108:109], v[144:145], v[108:109], 1.0 op_sel_hi:[1,1,0]
	v_pk_mul_f32 v[112:113], v[50:51], v[112:113]
	v_pk_fma_f32 v[110:111], v[154:155], v[110:111], 1.0 op_sel_hi:[1,1,0]
	v_pk_mul_f32 v[108:109], v[152:153], v[108:109]
	v_pk_mul_f32 v[114:115], v[136:137], v[114:115]
	v_pk_mul_f32 v[110:111], v[150:151], v[110:111]
	v_mul_f32_e32 v152, v131, v113
	v_mul_f32_e32 v153, v139, v121
	v_pk_mul_f32 v[162:163], v[138:139], v[116:117]
	v_add_u32_e32 v49, s50, v168
	v_fma_f32 v144, v130, v112, v152
	v_fma_f32 v145, v138, v120, v153
	v_mul_f32_e32 v154, v129, v115
	v_mul_f32_e32 v155, v141, v123
	ds_read_b128 v[146:149], v49
	v_fma_f32 v150, v128, v114, v154
	v_fma_f32 v151, v140, v122, v155
	v_mov_b32_e32 v155, v132
	v_mov_b32_e32 v157, v162
	v_mov_b32_e32 v132, v139
	v_mov_b32_e32 v162, v117
	v_pk_mul_f32 v[160:161], v[140:141], v[118:119]
	v_mov_b32_e32 v154, v138
	v_mov_b32_e32 v156, v116
	v_pk_mul_f32 v[132:133], v[132:133], v[162:163]
	v_pk_mul_f32 v[152:153], v[130:131], v[108:109]
	v_pk_fma_f32 v[132:133], v[154:155], v[156:157], v[132:133]
	v_pk_mov_b32 v[154:155], v[140:141], v[134:135] op_sel:[1,0]
	v_pk_mov_b32 v[156:157], v[118:119], v[160:161] op_sel:[1,0]
	v_mov_b32_e32 v134, v140
	v_mov_b32_e32 v160, v118
	v_pk_mul_f32 v[134:135], v[134:135], v[160:161]
	v_pk_add_f32 v[144:145], v[144:145], v[150:151]
	v_pk_fma_f32 v[134:135], v[154:155], v[156:157], v[134:135]
	v_mov_b32_e32 v155, v152
	v_pk_add_f32 v[132:133], v[132:133], v[134:135]
	s_waitcnt lgkmcnt(0)
	v_mov_b32_e32 v135, v146
	v_mov_b32_e32 v146, v131
	v_mov_b32_e32 v152, v109
	v_add_f32_e32 v49, 0, v145
	v_pk_mul_f32 v[150:151], v[128:129], v[110:111]
	v_mov_b32_e32 v134, v130
	v_mov_b32_e32 v154, v108
	v_pk_mul_f32 v[146:147], v[146:147], v[152:153]
	v_add_f32_e32 v49, v144, v49
	v_pk_fma_f32 v[134:135], v[134:135], v[154:155], v[146:147]
	v_pk_mov_b32 v[146:147], v[128:129], v[148:149] op_sel:[1,0]
	v_pk_mov_b32 v[152:153], v[110:111], v[150:151] op_sel:[1,0]
	v_mov_b32_e32 v148, v128
	v_mov_b32_e32 v150, v110
	s_and_b32 s44, s52, 1
	v_add_f32_dpp v49, v49, v49 row_half_mirror row_mask:0xf bank_mask:0xf bound_ctrl:1
	v_pk_mul_f32 v[148:149], v[148:149], v[150:151]
	s_lshl_b32 s2, s44, 13
	v_add_f32_dpp v49, v49, v49 quad_perm:[3,2,1,0] row_mask:0xf bank_mask:0xf bound_ctrl:1
	v_pk_fma_f32 v[146:147], v[146:147], v[152:153], v[148:149]
	v_pk_add_f32 v[132:133], v[132:133], 0 op_sel_hi:[1,0]
	v_add_f32_dpp v144, v49, v49 quad_perm:[1,0,3,2] row_mask:0xf bank_mask:0xf bound_ctrl:1
	v_pk_add_f32 v[134:135], v[134:135], v[146:147]
	v_add_u32_e32 v145, s2, v172
	v_mov_b32_e32 v162, 0
	v_mov_b32_e32 v163, 0
	v_mov_b32_e32 v164, v48
	v_mov_b32_e32 v165, v48
	v_pk_add_f32 v[132:133], v[132:133], v[134:135]
	v_mov_b32_e32 v134, v48
	v_mov_b32_e32 v135, v48
	v_pk_mul_f32 v[156:157], v[142:143], v[144:145] op_sel_hi:[1,0]
	v_pk_mul_f32 v[154:155], v[194:195], v[144:145] op_sel_hi:[1,0]
	s_waitcnt vmcnt(0)
	v_mov_b32_dpp v162, v8 row_shr:8 row_mask:0xf bank_mask:0xf
	v_mov_b32_dpp v163, v9 row_shr:8 row_mask:0xf bank_mask:0xf
	v_mov_b32_dpp v164, v10 row_shr:8 row_mask:0xf bank_mask:0xf
	v_mov_b32_dpp v165, v11 row_shr:8 row_mask:0xf bank_mask:0xf
	v_mov_b32_dpp v134, v132 row_half_mirror row_mask:0xf bank_mask:0xf
	v_mov_b32_dpp v135, v133 row_half_mirror row_mask:0xf bank_mask:0xf
	v_xor_b32_e32 v160, 0x80000000, v142
	v_xor_b32_e32 v161, 0x80000000, v143
	v_xor_b32_e32 v158, 0x80000000, v194
	v_xor_b32_e32 v159, 0x80000000, v195
	v_pk_fma_f32 v[154:155], v[10:11], v[140:141], v[154:155] neg_lo:[0,0,1] neg_hi:[0,0,1]
	v_pk_fma_f32 v[156:157], v[8:9], v[138:139], v[156:157] neg_lo:[0,0,1] neg_hi:[0,0,1]
	v_pk_mul_f32 v[138:139], v[142:143], v[162:163] neg_lo:[1,0] neg_hi:[1,0]
	v_pk_mul_f32 v[140:141], v[194:195], v[164:165] neg_lo:[1,0] neg_hi:[1,0]
	v_pk_add_f32 v[132:133], v[132:133], v[134:135]
	v_mov_b32_e32 v134, v48
	v_mov_b32_e32 v135, v48
	v_cndmask_b32_e64 v194, v141, v159, s[0:1]
	v_cndmask_b32_e64 v195, v140, v158, s[0:1]
	v_cndmask_b32_e64 v197, v139, v161, s[0:1]
	v_cndmask_b32_e64 v198, v138, v160, s[0:1]
	v_pk_mul_f32 v[138:139], v[156:157], v[162:163]
	v_pk_mul_f32 v[140:141], v[154:155], v[164:165]
	v_mov_b32_dpp v134, v132 quad_perm:[3,2,1,0] row_mask:0xf bank_mask:0xf
	v_mov_b32_dpp v135, v133 quad_perm:[3,2,1,0] row_mask:0xf bank_mask:0xf
	v_add_u32_e32 v193, s2, v171
	v_cndmask_b32_e64 v141, v141, v155, s[0:1]
	v_cndmask_b32_e64 v199, v140, v154, s[0:1]
	v_cndmask_b32_e64 v140, v139, v157, s[0:1]
	v_cndmask_b32_e64 v200, v138, v156, s[0:1]
	v_mov_b32_e32 v49, v48
	v_pk_add_f32 v[132:133], v[132:133], v[134:135]
	v_mov_b32_e32 v134, 0
	v_mov_b32_e32 v135, 0
	v_lshl_add_u32 v196, s44, 14, v173
	v_mov_b32_e32 v146, 0
	v_mov_b32_e32 v149, 0
	v_mov_b32_e32 v148, 0
	v_mov_b32_e32 v147, 0
	v_mov_b32_e32 v150, 0
	v_mov_b32_e32 v153, 0
	v_mov_b32_e32 v152, 0
	v_mov_b32_e32 v151, 0
	v_cvt_pk_bf16_f32 v138, v198, v197
	v_cvt_pk_bf16_f32 v139, v195, v194
	v_cvt_pk_bf16_f32 v140, v200, v140
	v_cvt_pk_bf16_f32 v141, v199, v141
	v_add_u32_e32 v194, v193, v183
	v_mov_b32_dpp v134, v132 quad_perm:[1,0,3,2] row_mask:0xf bank_mask:0xf
	v_mov_b32_dpp v135, v133 quad_perm:[1,0,3,2] row_mask:0xf bank_mask:0xf
	v_mov_b32_dpp v146, v120 row_shr:8 row_mask:0xf bank_mask:0xf
	v_mov_b32_dpp v149, v116 row_shr:8 row_mask:0xf bank_mask:0xf
	v_mov_b32_dpp v148, v121 row_shr:8 row_mask:0xf bank_mask:0xf
	v_mov_b32_dpp v147, v117 row_shr:8 row_mask:0xf bank_mask:0xf
	v_mov_b32_dpp v150, v122 row_shr:8 row_mask:0xf bank_mask:0xf
	v_mov_b32_dpp v153, v118 row_shr:8 row_mask:0xf bank_mask:0xf
	v_mov_b32_dpp v152, v123 row_shr:8 row_mask:0xf bank_mask:0xf
	v_mov_b32_dpp v151, v119 row_shr:8 row_mask:0xf bank_mask:0xf
	ds_write2_b64 v194, v[138:139], v[140:141] offset1:16
	v_add_u32_e32 v195, v145, v167
	v_add_u32_e32 v194, v196, v167
	v_mov_b64_e32 v[140:141], v[48:49]
	v_mov_b64_e32 v[138:139], v[48:49]
	s_and_saveexec_b64 s[14:15], s[4:5]
	s_cbranch_execz .LBB0_799
	v_pk_mul_f32 v[140:141], v[10:11], v[164:165]
	v_pk_mul_f32 v[138:139], v[8:9], v[162:163]
	ds_write_b128 v195, v[138:141] offset:16384
	v_mul_f32_e32 v140, v10, v150
	v_mul_f32_e32 v141, v11, v152
	v_mul_f32_e32 v138, v8, v146
	v_mul_f32_e32 v139, v9, v148
	ds_write_b128 v194, v[138:141] offset:32768
	v_mul_f32_e32 v140, v10, v153
	v_mul_f32_e32 v141, v11, v151
	v_mul_f32_e32 v138, v8, v149
	v_mul_f32_e32 v139, v9, v147
	ds_write_b128 v194, v[138:141] offset:33024
	ds_write_b128 v194, v[120:123] offset:33280
	ds_write_b128 v194, v[116:119] offset:33536
	v_pk_mul_f32 v[116:117], v[142:143], v[146:147] neg_lo:[1,0] neg_hi:[1,0]
	v_pk_mul_f32 v[118:119], v[158:159], v[150:151]
	v_pk_fma_f32 v[116:117], v[160:161], v[148:149], v[116:117] op_sel:[1,0,0] op_sel_hi:[0,1,1]
	v_pk_fma_f32 v[118:119], v[158:159], v[152:153], v[118:119] op_sel:[1,0,0] op_sel_hi:[0,1,1]
	v_pk_add_f32 v[116:117], v[116:117], v[118:119]
	v_pk_mul_f32 v[118:119], v[154:155], v[150:151]
	v_pk_add_f32 v[140:141], v[116:117], 0 op_sel_hi:[1,0]
	v_pk_mul_f32 v[116:117], v[156:157], v[146:147]
	v_pk_fma_f32 v[118:119], v[154:155], v[152:153], v[118:119] op_sel:[1,0,0] op_sel_hi:[0,1,1]
	v_pk_fma_f32 v[116:117], v[156:157], v[148:149], v[116:117] op_sel:[1,0,0] op_sel_hi:[0,1,1]
	v_pk_add_f32 v[116:117], v[116:117], v[118:119]
	s_nop 0
	v_pk_add_f32 v[138:139], v[116:117], 0 op_sel_hi:[1,0]
.LBB0_799:
	s_or_b64 exec, exec, s[14:15]
	s_mul_hi_u32 s2, s52, 0xaaaaaaab
	s_lshr_b32 s2, s2, 1
	s_mul_i32 s2, s2, 3
	v_lshlrev_b32_e32 v120, 16, v76
	v_and_b32_e32 v121, 0xffff0000, v76
	v_lshlrev_b32_e32 v122, 16, v77
	v_and_b32_e32 v123, 0xffff0000, v77
	v_lshlrev_b32_e32 v49, 16, v84
	v_and_b32_e32 v142, 0xffff0000, v84
	v_lshlrev_b32_e32 v146, 16, v85
	v_and_b32_e32 v147, 0xffff0000, v85
	s_sub_i32 s2, s52, s2
	v_sub_f32_e32 v143, v142, v121
	v_sub_f32_e32 v142, v49, v120
	v_sub_f32_e32 v147, v147, v123
	v_sub_f32_e32 v146, v146, v122
	s_lshl_b32 s14, s2, 13
	v_mov_b32_e32 v145, v144
	v_pk_fma_f32 v[106:107], v[146:147], v[106:107], v[122:123]
	v_pk_fma_f32 v[104:105], v[142:143], v[104:105], v[120:121]
	v_add_u32_e32 v49, s14, v177
	ds_write_b128 v49, v[104:107]
	v_mov_b32_e32 v104, v144
	v_mov_b32_e32 v105, v144
	v_pk_mul_f32 v[120:121], v[50:51], v[144:145]
	v_mov_b32_e32 v144, 0
	v_mov_b32_e32 v145, 0
	v_mov_b32_e32 v146, 0
	v_mov_b32_e32 v147, 0
	v_pk_mul_f32 v[122:123], v[136:137], v[104:105]
	v_mov_b32_dpp v144, v12 row_shr:8 row_mask:0xf bank_mask:0xf
	v_mov_b32_dpp v145, v13 row_shr:8 row_mask:0xf bank_mask:0xf
	v_mov_b32_dpp v146, v14 row_shr:8 row_mask:0xf bank_mask:0xf
	v_mov_b32_dpp v147, v15 row_shr:8 row_mask:0xf bank_mask:0xf
	v_xor_b32_e32 v137, 0x80000000, v137
	v_xor_b32_e32 v136, 0x80000000, v136
	v_xor_b32_e32 v142, 0x80000000, v50
	v_xor_b32_e32 v143, 0x80000000, v51
	v_pk_fma_f32 v[120:121], v[12:13], v[130:131], v[120:121] neg_lo:[0,0,1] neg_hi:[0,0,1]
	v_pk_fma_f32 v[122:123], v[14:15], v[128:129], v[122:123] neg_lo:[0,0,1] neg_hi:[0,0,1]
	v_pk_mul_f32 v[128:129], v[136:137], v[146:147]
	v_pk_mul_f32 v[130:131], v[50:51], v[144:145] neg_lo:[1,0] neg_hi:[1,0]
	v_lshlrev_b32_e32 v116, 16, v96
	v_and_b32_e32 v117, 0xffff0000, v96
	v_lshlrev_b32_e32 v118, 16, v97
	v_and_b32_e32 v119, 0xffff0000, v97
	v_add_u32_e32 v148, s14, v169
	v_cndmask_b32_e64 v149, v129, v137, s[0:1]
	v_cndmask_b32_e64 v150, v128, v136, s[0:1]
	v_cndmask_b32_e64 v151, v131, v143, s[0:1]
	v_cndmask_b32_e64 v152, v130, v142, s[0:1]
	v_pk_mul_f32 v[128:129], v[120:121], v[144:145]
	v_pk_mul_f32 v[130:131], v[122:123], v[146:147]
	ds_write_b128 v148, v[116:119]
	v_mov_b32_e32 v104, 0
	v_mov_b32_e32 v107, 0
	v_mov_b32_e32 v106, 0
	v_mov_b32_e32 v105, 0
	v_mov_b32_e32 v116, 0
	v_mov_b32_e32 v119, 0
	v_mov_b32_e32 v118, 0
	v_mov_b32_e32 v117, 0
	v_cndmask_b32_e64 v131, v131, v123, s[0:1]
	v_cndmask_b32_e64 v153, v130, v122, s[0:1]
	v_cndmask_b32_e64 v130, v129, v121, s[0:1]
	v_cndmask_b32_e64 v154, v128, v120, s[0:1]
	v_mov_b32_dpp v104, v112 row_shr:8 row_mask:0xf bank_mask:0xf
	v_mov_b32_dpp v107, v108 row_shr:8 row_mask:0xf bank_mask:0xf
	v_mov_b32_dpp v106, v113 row_shr:8 row_mask:0xf bank_mask:0xf
	v_mov_b32_dpp v105, v109 row_shr:8 row_mask:0xf bank_mask:0xf
	v_mov_b32_dpp v116, v114 row_shr:8 row_mask:0xf bank_mask:0xf
	v_mov_b32_dpp v119, v110 row_shr:8 row_mask:0xf bank_mask:0xf
	v_mov_b32_dpp v118, v115 row_shr:8 row_mask:0xf bank_mask:0xf
	v_mov_b32_dpp v117, v111 row_shr:8 row_mask:0xf bank_mask:0xf
	v_cvt_pk_bf16_f32 v128, v152, v151
	v_cvt_pk_bf16_f32 v129, v150, v149
	v_cvt_pk_bf16_f32 v130, v154, v130
	v_cvt_pk_bf16_f32 v131, v153, v131
	v_add_u32_e32 v149, v193, v184
	ds_write2_b64 v149, v[128:129], v[130:131] offset1:16
	s_and_saveexec_b64 s[14:15], s[4:5]
	s_cbranch_execz .LBB0_801
	v_pk_mul_f32 v[130:131], v[14:15], v[146:147]
	v_pk_mul_f32 v[128:129], v[12:13], v[144:145]
	ds_write_b128 v195, v[128:131] offset:16400
	v_mul_f32_e32 v130, v14, v116
	v_mul_f32_e32 v131, v15, v118
	v_mul_f32_e32 v128, v12, v104
	v_mul_f32_e32 v129, v13, v106
	ds_write_b128 v194, v[128:131] offset:32784
	v_mul_f32_e32 v130, v14, v119
	v_mul_f32_e32 v131, v15, v117
	v_mul_f32_e32 v128, v12, v107
	v_mul_f32_e32 v129, v13, v105
	ds_write_b128 v194, v[128:131] offset:33040
	ds_write_b128 v194, v[112:115] offset:33296
	ds_write_b128 v194, v[108:111] offset:33552
	v_pk_mul_f32 v[50:51], v[50:51], v[104:105] neg_lo:[1,0] neg_hi:[1,0]
	v_pk_mul_f32 v[108:109], v[136:137], v[116:117]
	v_pk_fma_f32 v[50:51], v[142:143], v[106:107], v[50:51] op_sel:[1,0,0] op_sel_hi:[0,1,1]
	v_pk_fma_f32 v[108:109], v[136:137], v[118:119], v[108:109] op_sel:[1,0,0] op_sel_hi:[0,1,1]
	v_pk_add_f32 v[50:51], v[50:51], v[108:109]
	s_nop 0
	v_pk_add_f32 v[140:141], v[140:141], v[50:51]
	v_pk_mul_f32 v[50:51], v[120:121], v[104:105]
	v_pk_mul_f32 v[104:105], v[122:123], v[116:117]
	v_pk_fma_f32 v[50:51], v[120:121], v[106:107], v[50:51] op_sel:[1,0,0] op_sel_hi:[0,1,1]
	v_pk_fma_f32 v[104:105], v[122:123], v[118:119], v[104:105] op_sel:[1,0,0] op_sel_hi:[0,1,1]
	v_pk_add_f32 v[50:51], v[50:51], v[104:105]
	s_nop 0
	v_pk_add_f32 v[138:139], v[138:139], v[50:51]
